# v60 + attention unit first tile: the 8 K fragments read up front into 8 register quads (counted waits) instead of read+wait per MFMA
# baseline (speedup 1.0000x reference)
.LBB0_425:
	s_lshl_b32 s9, s65, 13
	v_lshlrev_b32_e32 v0, 10, v196
	v_lshlrev_b32_e32 v1, 4, v220
	s_add_i32 s9, s9, 0
	v_add3_u32 v224, s9, v0, v1
	v_mov_b32_e32 v0, v129
	s_waitcnt vmcnt(2) lgkmcnt(0)
	s_barrier
	v_or_b32_e32 v51, s38, v220
	v_mov_b32_e32 v14, v0
	v_mov_b32_e32 v15, v0
	v_mov_b32_e32 v1, v0
	v_mov_b32_e32 v2, v0
	v_mov_b32_e32 v3, v0
	v_mov_b32_e32 v4, v0
	v_mov_b32_e32 v5, v0
	v_mov_b32_e32 v6, v0
	v_mov_b32_e32 v7, v0
	v_mov_b32_e32 v8, v0
	v_mov_b32_e32 v9, v0
	v_mov_b32_e32 v10, v0
	v_mov_b32_e32 v11, v0
	v_mov_b32_e32 v12, v0
	v_mov_b32_e32 v13, v0
	v_mov_b64_e32 v[30:31], v[14:15]
	v_mov_b64_e32 v[28:29], v[12:13]
	v_mov_b64_e32 v[26:27], v[10:11]
	v_mov_b64_e32 v[24:25], v[8:9]
	v_mov_b64_e32 v[22:23], v[6:7]
	v_mov_b64_e32 v[20:21], v[4:5]
	v_mov_b64_e32 v[18:19], v[2:3]
	v_mov_b64_e32 v[16:17], v[0:1]
	ds_read_b128 v[52:55], v224
	ds_read_b128 v[96:99], v224 offset:512
	ds_read_b128 v[100:103], v224 offset:2048
	ds_read_b128 v[104:107], v224 offset:2560
	ds_read_b128 v[108:111], v224 offset:4096
	ds_read_b128 v[116:119], v224 offset:4608
	ds_read_b128 v[120:123], v224 offset:6144
	ds_read_b128 v[124:127], v224 offset:6656
	v_or_b32_e32 v223, s68, v51
	s_cmpk_gt_u32 s68, 0xbf
	v_lshlrev_b32_e32 v219, 2, v196
	s_waitcnt vmcnt(3) lgkmcnt(7)
	v_mfma_f32_32x32x16_bf16 v[32:47], v[52:55], v[154:157], v[16:31]
	s_waitcnt lgkmcnt(6)
	v_mfma_f32_32x32x16_bf16 v[16:31], v[96:99], v[154:157], v[16:31]
	s_waitcnt vmcnt(2) lgkmcnt(5)
	v_mfma_f32_32x32x16_bf16 v[32:47], v[100:103], v[150:153], v[32:47]
	s_waitcnt lgkmcnt(4)
	v_mfma_f32_32x32x16_bf16 v[16:31], v[104:107], v[150:153], v[16:31]
	s_waitcnt vmcnt(1) lgkmcnt(3)
	v_mfma_f32_32x32x16_bf16 v[32:47], v[108:111], v[146:149], v[32:47]
	s_waitcnt lgkmcnt(2)
	v_mfma_f32_32x32x16_bf16 v[16:31], v[116:119], v[146:149], v[16:31]
	s_waitcnt vmcnt(0) lgkmcnt(1)
	v_mfma_f32_32x32x16_bf16 v[32:47], v[120:123], v[142:145], v[32:47]
	s_waitcnt lgkmcnt(0)
	v_mfma_f32_32x32x16_bf16 v[16:31], v[124:127], v[142:145], v[16:31]
	s_cbranch_scc1 .LBB0_427
	v_lshlrev_b32_e32 v51, 2, v196
	v_sub_u32_e32 v51, v223, v51
	v_mov_b32_e32 v56, v51
	s_cmp_eq_u32 s8, 0
	v_sub_u32_e32 v52, 0x100, v56
	v_and_b32_e32 v53, 3, v52
	v_and_b32_e32 v52, 0x3ffffffc, v52
	v_mul_u32_u24_e32 v53, 0x620, v53
	v_lshlrev_b32_e32 v52, 2, v52
	v_add3_u32 v52, s12, v53, v52
	ds_read_b128 v[52:55], v52
	s_cselect_b32 s9, 0, 0xfffe7960
	v_cmp_le_i32_e32 vcc, s9, v56
	v_subrev_u32_e32 v58, 32, v56
	v_subrev_u32_e32 v57, 33, v56
	s_waitcnt lgkmcnt(0)
	v_add_f32_e32 v32, v32, v52
	v_cndmask_b32_e32 v32, v212, v32, vcc
	v_cmp_lt_i32_e32 vcc, s9, v56
	v_add_f32_e32 v33, v33, v53
	v_add_u32_e32 v53, -2, v56
	v_cndmask_b32_e32 v33, v212, v33, vcc
	v_add_u32_e32 v52, -3, v56
	v_pk_add_f32 v[34:35], v[34:35], v[54:55]
	v_cmp_le_i32_e32 vcc, s9, v53
	s_nop 1
	v_cndmask_b32_e32 v34, v212, v34, vcc
	v_cmp_le_i32_e32 vcc, s9, v52
	v_sub_u32_e32 v52, 0x120, v56
	v_and_b32_e32 v53, 3, v52
	v_and_b32_e32 v52, 0x3ffffffc, v52
	v_mul_u32_u24_e32 v53, 0x620, v53
	v_lshlrev_b32_e32 v52, 2, v52
	v_add3_u32 v52, s12, v53, v52
	ds_read_b128 v[52:55], v52
	v_cndmask_b32_e32 v35, v212, v35, vcc
	v_cmp_le_i32_e32 vcc, s9, v58
	s_waitcnt lgkmcnt(0)
	v_pk_add_f32 v[16:17], v[16:17], v[52:53]
	s_nop 0
	v_cndmask_b32_e32 v16, v212, v16, vcc
	v_cmp_le_i32_e32 vcc, s9, v57
	v_subrev_u32_e32 v53, 34, v56
	v_subrev_u32_e32 v52, 35, v56
	v_cndmask_b32_e32 v17, v212, v17, vcc
	v_pk_add_f32 v[18:19], v[18:19], v[54:55]
	v_cmp_le_i32_e32 vcc, s9, v53
	v_add_u32_e32 v56, -8, v51
	s_nop 0
	v_cndmask_b32_e32 v18, v212, v18, vcc
	v_cmp_le_i32_e32 vcc, s9, v52
	v_sub_u32_e32 v52, 0x100, v56
	v_and_b32_e32 v53, 3, v52
	v_and_b32_e32 v52, 0x3ffffffc, v52
	v_mul_u32_u24_e32 v53, 0x620, v53
	v_lshlrev_b32_e32 v52, 2, v52
	v_add3_u32 v52, s12, v53, v52
	ds_read_b128 v[52:55], v52
	v_cndmask_b32_e32 v19, v212, v19, vcc
	v_cmp_le_i32_e32 vcc, s9, v56
	v_subrev_u32_e32 v58, 32, v56
	v_subrev_u32_e32 v57, 33, v56
	s_waitcnt lgkmcnt(0)
	v_add_f32_e32 v36, v36, v52
	v_cndmask_b32_e32 v36, v212, v36, vcc
	v_cmp_lt_i32_e32 vcc, s9, v56
	v_add_f32_e32 v37, v37, v53
	v_add_u32_e32 v53, -2, v56
	v_cndmask_b32_e32 v37, v212, v37, vcc
	v_add_u32_e32 v52, -3, v56
	v_pk_add_f32 v[38:39], v[38:39], v[54:55]
	v_cmp_le_i32_e32 vcc, s9, v53
	s_nop 1
	v_cndmask_b32_e32 v38, v212, v38, vcc
	v_cmp_le_i32_e32 vcc, s9, v52
	v_sub_u32_e32 v52, 0x120, v56
	v_and_b32_e32 v53, 3, v52
	v_and_b32_e32 v52, 0x3ffffffc, v52
	v_mul_u32_u24_e32 v53, 0x620, v53
	v_lshlrev_b32_e32 v52, 2, v52
	v_add3_u32 v52, s12, v53, v52
	ds_read_b128 v[52:55], v52
	v_cndmask_b32_e32 v39, v212, v39, vcc
	v_cmp_le_i32_e32 vcc, s9, v58
	s_waitcnt lgkmcnt(0)
	v_pk_add_f32 v[20:21], v[20:21], v[52:53]
	s_nop 0
	v_cndmask_b32_e32 v20, v212, v20, vcc
	v_cmp_le_i32_e32 vcc, s9, v57
	v_subrev_u32_e32 v53, 34, v56
	v_subrev_u32_e32 v52, 35, v56
	v_cndmask_b32_e32 v21, v212, v21, vcc
	v_pk_add_f32 v[22:23], v[22:23], v[54:55]
	v_cmp_le_i32_e32 vcc, s9, v53
	v_add_u32_e32 v56, -16, v51
	v_subrev_u32_e32 v51, 24, v51
	v_cndmask_b32_e32 v22, v212, v22, vcc
	v_cmp_le_i32_e32 vcc, s9, v52
	v_sub_u32_e32 v52, 0x100, v56
	v_and_b32_e32 v53, 3, v52
	v_and_b32_e32 v52, 0x3ffffffc, v52
	v_mul_u32_u24_e32 v53, 0x620, v53
	v_lshlrev_b32_e32 v52, 2, v52
	v_add3_u32 v52, s12, v53, v52
	ds_read_b128 v[52:55], v52
	v_cndmask_b32_e32 v23, v212, v23, vcc
	v_cmp_le_i32_e32 vcc, s9, v56
	v_subrev_u32_e32 v58, 32, v56
	v_subrev_u32_e32 v57, 33, v56
	s_waitcnt lgkmcnt(0)
	v_add_f32_e32 v40, v40, v52
	v_cndmask_b32_e32 v40, v212, v40, vcc
	v_cmp_lt_i32_e32 vcc, s9, v56
	v_add_f32_e32 v41, v41, v53
	v_add_u32_e32 v53, -2, v56
	v_cndmask_b32_e32 v41, v212, v41, vcc
	v_add_u32_e32 v52, -3, v56
	v_pk_add_f32 v[42:43], v[42:43], v[54:55]
	v_cmp_le_i32_e32 vcc, s9, v53
	s_nop 1
	v_cndmask_b32_e32 v42, v212, v42, vcc
	v_cmp_le_i32_e32 vcc, s9, v52
	v_sub_u32_e32 v52, 0x120, v56
	v_and_b32_e32 v53, 3, v52
	v_and_b32_e32 v52, 0x3ffffffc, v52
	v_mul_u32_u24_e32 v53, 0x620, v53
	v_lshlrev_b32_e32 v52, 2, v52
	v_add3_u32 v52, s12, v53, v52
	ds_read_b128 v[52:55], v52
	v_cndmask_b32_e32 v43, v212, v43, vcc
	v_cmp_le_i32_e32 vcc, s9, v58
	s_waitcnt lgkmcnt(0)
	v_pk_add_f32 v[24:25], v[24:25], v[52:53]
	s_nop 0
	v_cndmask_b32_e32 v24, v212, v24, vcc
	v_cmp_le_i32_e32 vcc, s9, v57
	v_subrev_u32_e32 v53, 34, v56
	v_subrev_u32_e32 v52, 35, v56
	v_cndmask_b32_e32 v25, v212, v25, vcc
	v_pk_add_f32 v[26:27], v[26:27], v[54:55]
	v_cmp_le_i32_e32 vcc, s9, v53
	v_subrev_u32_e32 v57, 32, v51
	v_subrev_u32_e32 v56, 33, v51
	v_cndmask_b32_e32 v26, v212, v26, vcc
	v_cmp_le_i32_e32 vcc, s9, v52
	v_sub_u32_e32 v52, 0x100, v51
	v_and_b32_e32 v53, 3, v52
	v_and_b32_e32 v52, 0x3ffffffc, v52
	v_mul_u32_u24_e32 v53, 0x620, v53
	v_lshlrev_b32_e32 v52, 2, v52
	v_add3_u32 v52, s12, v53, v52
	ds_read_b128 v[52:55], v52
	v_cndmask_b32_e32 v27, v212, v27, vcc
	v_cmp_le_i32_e32 vcc, s9, v51
	s_waitcnt lgkmcnt(0)
	v_add_f32_e32 v44, v44, v52
	v_cndmask_b32_e32 v44, v212, v44, vcc
	v_cmp_lt_i32_e32 vcc, s9, v51
	v_add_f32_e32 v45, v45, v53
	v_add_u32_e32 v53, -2, v51
	v_cndmask_b32_e32 v45, v212, v45, vcc
	v_add_u32_e32 v52, -3, v51
	v_pk_add_f32 v[46:47], v[46:47], v[54:55]
	v_cmp_le_i32_e32 vcc, s9, v53
	s_nop 1
	v_cndmask_b32_e32 v46, v212, v46, vcc
	v_cmp_le_i32_e32 vcc, s9, v52
	v_sub_u32_e32 v52, 0x120, v51
	v_and_b32_e32 v53, 3, v52
	v_and_b32_e32 v52, 0x3ffffffc, v52
	v_mul_u32_u24_e32 v53, 0x620, v53
	v_lshlrev_b32_e32 v52, 2, v52
	v_add3_u32 v52, s12, v53, v52
	ds_read_b128 v[52:55], v52
	v_cndmask_b32_e32 v47, v212, v47, vcc
	v_cmp_le_i32_e32 vcc, s9, v57
	s_waitcnt lgkmcnt(0)
	v_pk_add_f32 v[28:29], v[28:29], v[52:53]
	s_nop 0
	v_cndmask_b32_e32 v28, v212, v28, vcc
	v_cmp_le_i32_e32 vcc, s9, v56
	v_subrev_u32_e32 v52, 35, v51
	v_subrev_u32_e32 v51, 34, v51
	v_cndmask_b32_e32 v29, v212, v29, vcc
	v_pk_add_f32 v[30:31], v[30:31], v[54:55]
	v_cmp_le_i32_e32 vcc, s9, v51
	s_nop 1
	v_cndmask_b32_e32 v30, v212, v30, vcc
	v_cmp_le_i32_e32 vcc, s9, v52
	s_nop 1
	v_cndmask_b32_e32 v31, v212, v31, vcc
